# baseline (speedup 1.0000x reference)
_Z6gat_k2PKDF16_S0_S0_PKfPf:
	s_load_dwordx8 s[4:11], s[0:1], 0x0
	s_load_dwordx2 s[12:13], s[0:1], 0x20
	v_readfirstlane_b32 s14, v0
	v_and_b32_e32 v46, 63, v0
	v_lshlrev_b32_e32 v1, 4, v46
	s_and_b32 s16, s2, 1
	s_bfe_u32 s17, s2, 0x40003
	s_lshl_b32 s17, s17, 2
	s_lshr_b32 s18, s2, 1
	s_lshr_b32 s15, s14, 6
	s_lshl_b32 s19, s16, 19
	s_lshl_b32 s23, s15, 16
	s_add_u32 s19, s19, s23
	s_lshl_b32 s23, s15, 11
	v_lshrrev_b32_e32 v48, 1, v46
	v_add_u32_e32 v48, s17, v48
	v_and_b32_e32 v48, 63, v48
	v_lshlrev_b32_e32 v48, 5, v48
	v_and_b32_e32 v49, 1, v46
	v_lshl_or_b32 v48, v49, 4, v48
	v_xor_b32_e32 v49, 0x400, v48
	v_add_u32_e32 v48, s23, v48
	v_add_u32_e32 v49, s23, v49
	s_mul_i32 s32, s15, 0x1900
	s_add_u32 s32, s32, 75776
	v_and_b32_e32 v44, 31, v0
	v_lshlrev_b32_e32 v45, 2, v44
	s_lshl_b32 s23, s18, 8
	v_add_u32_e32 v45, s23, v45
	s_waitcnt lgkmcnt(0)
	global_load_dword v42, v45, s[10:11]
	global_load_dword v43, v45, s[10:11] offset:128
	s_mov_b32 m0, s32
	s_add_u32 s33, s32, 0x400
	global_load_lds_dwordx4 v48, s[6:7]
	s_mov_b32 m0, s33
	s_add_u32 s34, s32, 0x800
	global_load_lds_dwordx4 v49, s[6:7]
	s_mov_b32 m0, s34
	s_add_u32 s35, s32, 0xc00
	global_load_lds_dwordx4 v48, s[8:9]
	s_mov_b32 m0, s35
	s_add_u32 s20, s4, s19
	global_load_lds_dwordx4 v49, s[8:9]
	s_addc_u32 s21, s5, 0
	s_add_u32 s23, s17, 0
	s_and_b32 s23, s23, 63
	s_lshl_b32 s23, s23, 10
	s_add_u32 s24, s20, s23
	s_addc_u32 s25, s21, 0
	global_load_dwordx4 v[64:67], v1, s[24:25]
	s_add_u32 s23, s17, 1
	s_and_b32 s23, s23, 63
	s_lshl_b32 s23, s23, 10
	s_add_u32 s24, s20, s23
	s_addc_u32 s25, s21, 0
	global_load_dwordx4 v[68:71], v1, s[24:25]
	s_add_u32 s23, s17, 2
	s_and_b32 s23, s23, 63
	s_lshl_b32 s23, s23, 10
	s_add_u32 s24, s20, s23
	s_addc_u32 s25, s21, 0
	global_load_dwordx4 v[72:75], v1, s[24:25]
	s_add_u32 s23, s17, 3
	s_and_b32 s23, s23, 63
	s_lshl_b32 s23, s23, 10
	s_add_u32 s24, s20, s23
	s_addc_u32 s25, s21, 0
	global_load_dwordx4 v[76:79], v1, s[24:25]
	s_add_u32 s23, s17, 4
	s_and_b32 s23, s23, 63
	s_lshl_b32 s23, s23, 10
	s_add_u32 s24, s20, s23
	s_addc_u32 s25, s21, 0
	global_load_dwordx4 v[80:83], v1, s[24:25]
	s_add_u32 s23, s17, 5
	s_and_b32 s23, s23, 63
	s_lshl_b32 s23, s23, 10
	s_add_u32 s24, s20, s23
	s_addc_u32 s25, s21, 0
	global_load_dwordx4 v[84:87], v1, s[24:25]
	s_add_u32 s23, s17, 6
	s_and_b32 s23, s23, 63
	s_lshl_b32 s23, s23, 10
	s_add_u32 s24, s20, s23
	s_addc_u32 s25, s21, 0
	global_load_dwordx4 v[88:91], v1, s[24:25]
	s_add_u32 s23, s17, 7
	s_and_b32 s23, s23, 63
	s_lshl_b32 s23, s23, 10
	s_add_u32 s24, s20, s23
	s_addc_u32 s25, s21, 0
	global_load_dwordx4 v[92:95], v1, s[24:25]
	v_accvgpr_write_b32 a0, 0
	v_accvgpr_write_b32 a1, 0
	v_accvgpr_write_b32 a2, 0
	v_accvgpr_write_b32 a3, 0
	v_accvgpr_write_b32 a4, 0
	v_accvgpr_write_b32 a5, 0
	v_accvgpr_write_b32 a6, 0
	v_accvgpr_write_b32 a7, 0
	v_accvgpr_write_b32 a8, 0
	v_accvgpr_write_b32 a9, 0
	v_accvgpr_write_b32 a10, 0
	v_accvgpr_write_b32 a11, 0
	v_accvgpr_write_b32 a12, 0
	v_accvgpr_write_b32 a13, 0
	v_accvgpr_write_b32 a14, 0
	v_accvgpr_write_b32 a15, 0
	v_accvgpr_write_b32 a16, 0
	v_accvgpr_write_b32 a17, 0
	v_accvgpr_write_b32 a18, 0
	v_accvgpr_write_b32 a19, 0
	v_accvgpr_write_b32 a20, 0
	v_accvgpr_write_b32 a21, 0
	v_accvgpr_write_b32 a22, 0
	v_accvgpr_write_b32 a23, 0
	v_accvgpr_write_b32 a24, 0
	v_accvgpr_write_b32 a25, 0
	v_accvgpr_write_b32 a26, 0
	v_accvgpr_write_b32 a27, 0
	v_accvgpr_write_b32 a28, 0
	v_accvgpr_write_b32 a29, 0
	v_accvgpr_write_b32 a30, 0
	v_accvgpr_write_b32 a31, 0
	v_accvgpr_write_b32 a32, 0
	v_accvgpr_write_b32 a33, 0
	v_accvgpr_write_b32 a34, 0
	v_accvgpr_write_b32 a35, 0
	v_accvgpr_write_b32 a36, 0
	v_accvgpr_write_b32 a37, 0
	v_accvgpr_write_b32 a38, 0
	v_accvgpr_write_b32 a39, 0
	v_mov_b32_e32 v2, 0
	v_mov_b32_e32 v3, 0
	v_mov_b32_e32 v4, 0
	v_mov_b32_e32 v5, 0
	v_add_u32_e32 v47, s32, v1
	ds_write_b128 v47, v[2:5] offset:4096
	ds_write_b128 v47, v[2:5] offset:5120
	s_waitcnt vmcnt(8)
	v_cvt_f16_f32_e32 v42, v42
	v_cvt_f16_f32_e32 v43, v43
	s_mov_b32 s28, 0x5040100
	v_perm_b32 v42, v42, v42, s28
	v_perm_b32 v43, v43, v43, s28
	v_lshrrev_b32_e32 v44, 5, v46
	v_and_b32_e32 v45, 15, v46
	v_bfe_u32 v47, v46, 4, 1
	v_cmp_eq_u32_e32 vcc, v45, v47
	v_lshlrev_b32_e32 v44, 4, v44
	v_add_u32_e32 v46, s32, v44
	v_add_u32_e32 v45, 0x800, v46
	v_mov_b32_e32 v47, s32
	v_add_u32_e32 v47, 0x1000, v47
	v_cndmask_b32_e32 v47, v47, v45, vcc
	s_waitcnt lgkmcnt(0)
	ds_read_b128 v[144:147], v46
	ds_read_b128 v[148:151], v46 offset:32
	ds_read_b128 v[160:163], v47
	ds_read_b128 v[152:155], v46 offset:64
	ds_read_b128 v[164:167], v47 offset:32
	s_add_u32 s27, s17, 8
	s_lshl_b32 s27, s27, 10
	s_add_u32 s29, s17, 60
	s_lshl_b32 s29, s29, 10
	s_movk_i32 s28, 0x1000
	s_mov_b32 s26, 0
	s_waitcnt lgkmcnt(4)
	v_pk_max_u16 v128, v144, v42
	v_pk_max_u16 v129, v145, v42
	v_pk_max_u16 v130, v146, v42
	v_pk_max_u16 v131, v147, v42
	v_pk_max_u16 v136, v144, v43
	v_pk_max_u16 v137, v145, v43
	v_pk_max_u16 v138, v146, v43
	v_pk_max_u16 v139, v147, v43
	s_mov_b32 s31, 0xfc00
	s_cmp_ge_u32 s15, 4
	s_cbranch_scc0 .Lk2_noprio
	s_setprio 1
.Lk2_noprio:
.Lk2_loop:
	s_and_b32 s23, s27, s31
	s_add_u32 s24, s20, s23
	s_addc_u32 s25, s21, 0
	s_add_u32 s27, s27, s28
	s_waitcnt vmcnt(7)
	s_waitcnt lgkmcnt(2)
	v_mfma_f32_32x32x16_f16 a[0:15], v[64:67], v[128:131], a[0:15]
	v_pk_max_u16 v132, v148, v42
	v_pk_max_u16 v133, v149, v42
	v_pk_max_u16 v134, v150, v42
	v_pk_max_u16 v135, v151, v42
	v_mfma_f32_32x32x16_f16 a[16:31], v[64:67], v[136:139], a[16:31]
	v_pk_max_u16 v140, v148, v43
	v_pk_max_u16 v141, v149, v43
	v_pk_max_u16 v142, v150, v43
	v_pk_max_u16 v143, v151, v43
	v_mfma_f32_16x16x32_f16 a[32:35], v[160:163], v[128:131], a[32:35]
	global_load_dwordx4 v[64:67], v1, s[24:25]
	ds_read_b128 v[156:159], v46 offset:96
	ds_read_b128 v[168:171], v47 offset:64
	v_mfma_f32_16x16x32_f16 a[36:39], v[160:163], v[136:139], a[36:39]
	s_waitcnt vmcnt(7)
	s_waitcnt lgkmcnt(2)
	v_mfma_f32_32x32x16_f16 a[0:15], v[68:71], v[132:135], a[0:15]
	v_pk_max_u16 v128, v152, v42
	v_pk_max_u16 v129, v153, v42
	v_pk_max_u16 v130, v154, v42
	v_pk_max_u16 v131, v155, v42
	v_mfma_f32_32x32x16_f16 a[16:31], v[68:71], v[140:143], a[16:31]
	v_pk_max_u16 v136, v152, v43
	v_pk_max_u16 v137, v153, v43
	v_pk_max_u16 v138, v154, v43
	v_pk_max_u16 v139, v155, v43
	v_mfma_f32_16x16x32_f16 a[32:35], v[164:167], v[132:135], a[32:35]
	global_load_dwordx4 v[68:71], v1, s[24:25] offset:1024
	ds_read_b128 v[144:147], v46 offset:128
	ds_read_b128 v[172:175], v47 offset:96
	v_mfma_f32_16x16x32_f16 a[36:39], v[164:167], v[140:143], a[36:39]
	s_waitcnt vmcnt(7)
	s_waitcnt lgkmcnt(2)
	v_mfma_f32_32x32x16_f16 a[0:15], v[72:75], v[128:131], a[0:15]
	v_pk_max_u16 v132, v156, v42
	v_pk_max_u16 v133, v157, v42
	v_pk_max_u16 v134, v158, v42
	v_pk_max_u16 v135, v159, v42
	v_mfma_f32_32x32x16_f16 a[16:31], v[72:75], v[136:139], a[16:31]
	v_pk_max_u16 v140, v156, v43
	v_pk_max_u16 v141, v157, v43
	v_pk_max_u16 v142, v158, v43
	v_pk_max_u16 v143, v159, v43
	v_mfma_f32_16x16x32_f16 a[32:35], v[168:171], v[128:131], a[32:35]
	global_load_dwordx4 v[72:75], v1, s[24:25] offset:2048
	ds_read_b128 v[148:151], v46 offset:160
	ds_read_b128 v[160:163], v47 offset:128
	v_mfma_f32_16x16x32_f16 a[36:39], v[168:171], v[136:139], a[36:39]
	s_waitcnt vmcnt(7)
	s_waitcnt lgkmcnt(2)
	v_mfma_f32_32x32x16_f16 a[0:15], v[76:79], v[132:135], a[0:15]
	v_pk_max_u16 v128, v144, v42
	v_pk_max_u16 v129, v145, v42
	v_pk_max_u16 v130, v146, v42
	v_pk_max_u16 v131, v147, v42
	v_mfma_f32_32x32x16_f16 a[16:31], v[76:79], v[140:143], a[16:31]
	v_pk_max_u16 v136, v144, v43
	v_pk_max_u16 v137, v145, v43
	v_pk_max_u16 v138, v146, v43
	v_pk_max_u16 v139, v147, v43
	v_mfma_f32_16x16x32_f16 a[32:35], v[172:175], v[132:135], a[32:35]
	global_load_dwordx4 v[76:79], v1, s[24:25] offset:3072
	ds_read_b128 v[152:155], v46 offset:192
	ds_read_b128 v[164:167], v47 offset:160
	v_mfma_f32_16x16x32_f16 a[36:39], v[172:175], v[140:143], a[36:39]
	s_and_b32 s23, s27, s31
	s_add_u32 s24, s20, s23
	s_addc_u32 s25, s21, 0
	s_add_u32 s27, s27, s28
	s_waitcnt vmcnt(7)
	s_waitcnt lgkmcnt(2)
	v_mfma_f32_32x32x16_f16 a[0:15], v[80:83], v[128:131], a[0:15]
	v_pk_max_u16 v132, v148, v42
	v_pk_max_u16 v133, v149, v42
	v_pk_max_u16 v134, v150, v42
	v_pk_max_u16 v135, v151, v42
	v_mfma_f32_32x32x16_f16 a[16:31], v[80:83], v[136:139], a[16:31]
	v_pk_max_u16 v140, v148, v43
	v_pk_max_u16 v141, v149, v43
	v_pk_max_u16 v142, v150, v43
	v_pk_max_u16 v143, v151, v43
	v_mfma_f32_16x16x32_f16 a[32:35], v[160:163], v[128:131], a[32:35]
	global_load_dwordx4 v[80:83], v1, s[24:25]
	ds_read_b128 v[156:159], v46 offset:224
	ds_read_b128 v[168:171], v47 offset:192
	v_mfma_f32_16x16x32_f16 a[36:39], v[160:163], v[136:139], a[36:39]
	s_waitcnt vmcnt(7)
	s_waitcnt lgkmcnt(2)
	v_mfma_f32_32x32x16_f16 a[0:15], v[84:87], v[132:135], a[0:15]
	v_pk_max_u16 v128, v152, v42
	v_pk_max_u16 v129, v153, v42
	v_pk_max_u16 v130, v154, v42
	v_pk_max_u16 v131, v155, v42
	v_mfma_f32_32x32x16_f16 a[16:31], v[84:87], v[140:143], a[16:31]
	v_pk_max_u16 v136, v152, v43
	v_pk_max_u16 v137, v153, v43
	v_pk_max_u16 v138, v154, v43
	v_pk_max_u16 v139, v155, v43
	v_mfma_f32_16x16x32_f16 a[32:35], v[164:167], v[132:135], a[32:35]
	global_load_dwordx4 v[84:87], v1, s[24:25] offset:1024
	ds_read_b128 v[144:147], v46 offset:256
	ds_read_b128 v[172:175], v47 offset:224
	v_mfma_f32_16x16x32_f16 a[36:39], v[164:167], v[140:143], a[36:39]
	s_waitcnt vmcnt(7)
	s_waitcnt lgkmcnt(2)
	v_mfma_f32_32x32x16_f16 a[0:15], v[88:91], v[128:131], a[0:15]
	v_pk_max_u16 v132, v156, v42
	v_pk_max_u16 v133, v157, v42
	v_pk_max_u16 v134, v158, v42
	v_pk_max_u16 v135, v159, v42
	v_mfma_f32_32x32x16_f16 a[16:31], v[88:91], v[136:139], a[16:31]
	v_pk_max_u16 v140, v156, v43
	v_pk_max_u16 v141, v157, v43
	v_pk_max_u16 v142, v158, v43
	v_pk_max_u16 v143, v159, v43
	v_mfma_f32_16x16x32_f16 a[32:35], v[168:171], v[128:131], a[32:35]
	global_load_dwordx4 v[88:91], v1, s[24:25] offset:2048
	ds_read_b128 v[148:151], v46 offset:288
	ds_read_b128 v[160:163], v47 offset:256
	v_mfma_f32_16x16x32_f16 a[36:39], v[168:171], v[136:139], a[36:39]
	s_waitcnt vmcnt(7)
	s_waitcnt lgkmcnt(2)
	v_mfma_f32_32x32x16_f16 a[0:15], v[92:95], v[132:135], a[0:15]
	v_pk_max_u16 v128, v144, v42
	v_pk_max_u16 v129, v145, v42
	v_pk_max_u16 v130, v146, v42
	v_pk_max_u16 v131, v147, v42
	v_mfma_f32_32x32x16_f16 a[16:31], v[92:95], v[140:143], a[16:31]
	v_pk_max_u16 v136, v144, v43
	v_pk_max_u16 v137, v145, v43
	v_pk_max_u16 v138, v146, v43
	v_pk_max_u16 v139, v147, v43
	v_mfma_f32_16x16x32_f16 a[32:35], v[172:175], v[132:135], a[32:35]
	global_load_dwordx4 v[92:95], v1, s[24:25] offset:3072
	ds_read_b128 v[152:155], v46 offset:320
	ds_read_b128 v[164:167], v47 offset:288
	v_add_u32_e32 v46, 256, v46
	v_add_u32_e32 v47, 256, v47
	v_mfma_f32_16x16x32_f16 a[36:39], v[172:175], v[140:143], a[36:39]
	s_add_u32 s26, s26, 1
	s_cmp_lt_u32 s26, 7
	s_cbranch_scc1 .Lk2_loop
	s_cmp_lt_u32 s26, 8
	s_cbranch_scc0 .Lk2_loopdone
	s_mov_b32 s27, s29
	s_mov_b32 s28, 0
	s_branch .Lk2_loop
